# stack15
# baseline (speedup 1.0000x reference)
_Z6k_rec2PKiS0_S0_PK15HIP_vector_typeIjLj4EEPKfS6_PS2_PS1_IjLj2EEPf:
	v_readfirstlane_b32 s90, v0
	s_lshr_b32 s90, s90, 8
	s_load_dwordx2 s[6:7], s[0:1], 0x0
	s_load_dwordx2 s[4:5], s[0:1], 0x28
	v_cmp_gt_u32_e32 vcc, 32, v0
	s_and_saveexec_b64 s[8:9], vcc
	v_mov_b32_e32 v1, 0x22000
	v_lshl_or_b32 v1, v0, 2, v1
	v_mov_b32_e32 v2, 0
	ds_write_b32 v1, v2
	s_or_b64 exec, exec, s[8:9]
	v_mov_b32_e32 v3, 0
	v_lshlrev_b32_e32 v2, 2, v0
	s_waitcnt lgkmcnt(0)
	v_lshl_add_u64 v[4:5], s[6:7], 0, v[2:3]
	s_movk_i32 s3, 0x1000
	v_or_b32_e32 v1, 0x400, v0
	v_add_co_u32_e32 v6, vcc, s3, v4
	v_lshlrev_b32_e32 v3, 2, v1
	s_nop 0
	v_addc_co_u32_e32 v7, vcc, 0, v5, vcc
	global_load_dword v68, v2, s[6:7]
	global_load_dword v69, v2, s[6:7] offset:2048
	global_load_dword v70, v3, s[6:7]
	global_load_dword v71, v[6:7], off offset:2048
	v_or_b32_e32 v165, 0x800, v0
	s_movk_i32 s3, 0x2000
	v_lshlrev_b32_e32 v6, 2, v165
	v_add_co_u32_e32 v2, vcc, s3, v4
	v_or_b32_e32 v232, 0xc00, v0
	s_nop 0
	v_addc_co_u32_e32 v3, vcc, 0, v5, vcc
	global_load_dword v72, v6, s[6:7]
	global_load_dword v73, v[2:3], off offset:2048
	v_lshlrev_b32_e32 v2, 2, v232
	global_load_dword v74, v2, s[6:7]
	s_movk_i32 s3, 0x3000
	v_add_co_u32_e32 v2, vcc, s3, v4
	s_ashr_i32 s3, s2, 31
	s_nop 0
	v_addc_co_u32_e32 v3, vcc, 0, v5, vcc
	global_load_dword v75, v[2:3], off offset:2048
	s_lshl_b64 s[6:7], s[2:3], 17
	s_add_u32 s4, s4, s6
	s_addc_u32 s5, s5, s7
	v_mbcnt_lo_u32_b32 v77, -1, 0
	v_mbcnt_hi_u32_b32 v77, -1, v77
	v_and_b32_e32 v83, 64, v77
	v_xor_b32_e32 v84, 32, v77
	v_add_u32_e32 v83, 64, v83
	v_cmp_lt_i32_e32 vcc, v84, v83
	v_xor_b32_e32 v85, 16, v77
	v_xor_b32_e32 v86, 8, v77
	v_cndmask_b32_e32 v84, v77, v84, vcc
	v_lshlrev_b32_e32 v234, 2, v84
	v_cmp_lt_i32_e32 vcc, v85, v83
	v_xor_b32_e32 v87, 4, v77
	v_xor_b32_e32 v88, 2, v77
	v_cndmask_b32_e32 v85, v77, v85, vcc
	v_lshlrev_b32_e32 v235, 2, v85
	v_cmp_lt_i32_e32 vcc, v86, v83
	v_xor_b32_e32 v89, 1, v77
	v_mov_b32_e32 v76, 0x20000
	v_cndmask_b32_e32 v86, v77, v86, vcc
	v_lshlrev_b32_e32 v236, 2, v86
	v_cmp_lt_i32_e32 vcc, v87, v83
	v_lshl_or_b32 v79, v1, 1, v76
	v_lshl_or_b32 v81, v165, 1, v76
	v_cndmask_b32_e32 v87, v77, v87, vcc
	v_cmp_lt_i32_e32 vcc, v88, v83
	v_lshlrev_b32_e32 v237, 2, v87
	v_lshl_or_b32 v76, v232, 1, v76
	v_cndmask_b32_e32 v88, v77, v88, vcc
	v_cmp_lt_i32_e32 vcc, v89, v83
	v_lshlrev_b32_e32 v238, 2, v88
	s_mov_b32 s3, 0
	v_cndmask_b32_e32 v77, v77, v89, vcc
	v_lshlrev_b32_e32 v239, 2, v77
	s_waitcnt vmcnt(7)
	v_lshlrev_b32_e32 v2, 1, v68
	s_waitcnt vmcnt(6)
	v_lshlrev_b32_e32 v4, 1, v69
	v_ashrrev_i32_e32 v3, 31, v2
	v_ashrrev_i32_e32 v5, 31, v4
	v_lshl_add_u64 v[10:11], v[2:3], 4, s[4:5]
	v_lshl_add_u64 v[20:21], v[4:5], 4, s[4:5]
	global_load_dwordx4 v[2:5], v[10:11], off offset:16
	global_load_dwordx4 v[6:9], v[10:11], off
	s_nop 0
	global_load_dwordx4 v[10:13], v[20:21], off offset:16
	global_load_dwordx4 v[14:17], v[20:21], off
	s_waitcnt vmcnt(9)
	v_lshlrev_b32_e32 v18, 1, v70
	v_ashrrev_i32_e32 v19, 31, v18
	v_lshl_add_u64 v[28:29], v[18:19], 4, s[4:5]
	global_load_dwordx4 v[18:21], v[28:29], off offset:16
	global_load_dwordx4 v[22:25], v[28:29], off
	s_waitcnt vmcnt(10)
	v_lshlrev_b32_e32 v26, 1, v71
	v_ashrrev_i32_e32 v27, 31, v26
	v_lshl_add_u64 v[36:37], v[26:27], 4, s[4:5]
	global_load_dwordx4 v[26:29], v[36:37], off offset:16
	global_load_dwordx4 v[30:33], v[36:37], off
	s_waitcnt vmcnt(11)
	v_lshlrev_b32_e32 v34, 1, v72
	v_ashrrev_i32_e32 v35, 31, v34
	v_lshl_add_u64 v[44:45], v[34:35], 4, s[4:5]
	global_load_dwordx4 v[34:37], v[44:45], off offset:16
	global_load_dwordx4 v[38:41], v[44:45], off
	s_waitcnt vmcnt(12)
	v_lshlrev_b32_e32 v42, 1, v73
	v_ashrrev_i32_e32 v43, 31, v42
	v_lshl_add_u64 v[52:53], v[42:43], 4, s[4:5]
	global_load_dwordx4 v[42:45], v[52:53], off offset:16
	global_load_dwordx4 v[46:49], v[52:53], off
	s_waitcnt vmcnt(13)
	v_lshlrev_b32_e32 v50, 1, v74
	v_ashrrev_i32_e32 v51, 31, v50
	v_lshl_add_u64 v[58:59], v[50:51], 4, s[4:5]
	global_load_dwordx4 v[50:53], v[58:59], off offset:16
	global_load_dwordx4 v[54:57], v[58:59], off
	s_waitcnt vmcnt(14)
	v_lshlrev_b32_e32 v58, 1, v75
	v_ashrrev_i32_e32 v59, 31, v58
	v_lshl_add_u64 v[66:67], v[58:59], 4, s[4:5]
	global_load_dwordx4 v[62:65], v[66:67], off
	global_load_dwordx4 v[58:61], v[66:67], off offset:16
	v_lshlrev_b32_e32 v67, 1, v0
	v_or_b32_e32 v233, 0x20000, v67
	s_load_dwordx4 s[8:11], s[0:1], 0x8
	s_load_dwordx2 s[14:15], s[0:1], 0x18
	s_load_dwordx2 s[12:13], s[0:1], 0x40
	s_load_dwordx2 s[6:7], s[0:1], 0x30
	v_or_b32_e32 v78, 0x20400, v67
	v_or_b32_e32 v80, 0x20c00, v67
	ds_write_b16 v233, v68
	ds_write_b16 v78, v69
	ds_write_b16 v79, v70
	ds_write_b16 v80, v71
	v_or_b32_e32 v82, 0x21400, v67
	v_or_b32_e32 v67, 0x21c00, v67
	ds_write_b16 v81, v72
	ds_write_b16 v82, v73
	ds_write_b16 v76, v74
	ds_write_b16 v67, v75
	v_mov_b32_e32 v246, v68
	v_mov_b32_e32 v247, v69
	v_mov_b32_e32 v248, v70
	v_mov_b32_e32 v249, v71
	v_mov_b32_e32 v250, v72
	v_mov_b32_e32 v251, v73
	v_mov_b32_e32 v252, v74
	v_mov_b32_e32 v253, v75
	v_and_b32_e32 v66, 63, v0
	v_cmp_eq_u32_e64 s[4:5], 0, v66
	s_waitcnt lgkmcnt(0)
	s_barrier
	s_waitcnt vmcnt(14)
	v_max3_f32 v84, |v6|, 0, |v7|
	v_max3_f32 v84, v84, |v8|, |v9|
	v_max3_f32 v84, v84, |v2|, |v3|
	v_max3_f32 v84, v84, |v4|, |v5|
	s_waitcnt vmcnt(12)
	v_max3_f32 v84, v84, |v14|, |v15|
	v_max3_f32 v84, v84, |v16|, |v17|
	v_max3_f32 v84, v84, |v10|, |v11|
	v_max3_f32 v84, v84, |v12|, |v13|
	s_waitcnt vmcnt(10)
	v_max3_f32 v84, v84, |v22|, |v23|
	v_max3_f32 v84, v84, |v24|, |v25|
	v_max3_f32 v84, v84, |v18|, |v19|
	v_max3_f32 v84, v84, |v20|, |v21|
	s_waitcnt vmcnt(8)
	v_max3_f32 v84, v84, |v30|, |v31|
	v_max3_f32 v84, v84, |v32|, |v33|
	v_max3_f32 v84, v84, |v26|, |v27|
	v_max3_f32 v84, v84, |v28|, |v29|
	s_waitcnt vmcnt(6)
	v_max3_f32 v84, v84, |v38|, |v39|
	v_max3_f32 v84, v84, |v40|, |v41|
	v_max3_f32 v84, v84, |v34|, |v35|
	v_max3_f32 v84, v84, |v36|, |v37|
	s_waitcnt vmcnt(4)
	v_max3_f32 v84, v84, |v46|, |v47|
	v_max3_f32 v84, v84, |v48|, |v49|
	v_max3_f32 v84, v84, |v42|, |v43|
	v_max3_f32 v84, v84, |v44|, |v45|
	s_waitcnt vmcnt(2)
	v_max3_f32 v84, v84, |v54|, |v55|
	v_max3_f32 v84, v84, |v56|, |v57|
	v_max3_f32 v84, v84, |v50|, |v51|
	v_max3_f32 v84, v84, |v52|, |v53|
	s_waitcnt vmcnt(1)
	v_max3_f32 v84, v84, |v62|, |v63|
	v_max3_f32 v84, v84, |v64|, |v65|
	s_waitcnt vmcnt(0)
	v_max3_f32 v84, v84, |v58|, |v59|
	v_max3_f32 v84, v84, |v60|, |v61|
	ds_bpermute_b32 v90, v234, v84
	s_waitcnt lgkmcnt(0)
	v_max_f32_e32 v85, v90, v90
	v_max_f32_e32 v84, v84, v85
	ds_bpermute_b32 v85, v235, v84
	s_waitcnt lgkmcnt(0)
	v_max_f32_e32 v85, v85, v85
	v_max_f32_e32 v84, v84, v85
	ds_bpermute_b32 v85, v236, v84
	s_waitcnt lgkmcnt(0)
	v_max_f32_e32 v83, v85, v85
	v_max_f32_e32 v83, v84, v83
	ds_bpermute_b32 v84, v237, v83
	s_waitcnt lgkmcnt(0)
	v_max_f32_e32 v68, v84, v84
	v_max_f32_e32 v68, v83, v68
	ds_bpermute_b32 v69, v238, v68
	s_waitcnt lgkmcnt(0)
	v_max_f32_e32 v67, v69, v69
	v_max_f32_e32 v67, v68, v67
	ds_bpermute_b32 v68, v239, v67
	s_and_saveexec_b64 s[16:17], s[4:5]
	s_cbranch_execz .LBB3_7
	s_waitcnt lgkmcnt(0)
	v_max_f32_e32 v68, v68, v68
	v_max_f32_e32 v67, v67, v67
	s_mov_b64 s[18:19], exec
	v_max_f32_e32 v67, v67, v68

.LBB3_36:
	s_setprio 0
	global_load_dwordx4 v[58:61], v[114:115], off
	global_load_dwordx4 v[62:65], v[116:117], off
	global_load_dwordx4 v[66:69], v[118:119], off
	global_load_dwordx4 v[70:73], v[120:121], off
	s_waitcnt lgkmcnt(1)
	v_bfe_u32 v76, v231, 23, 8
	s_cmp_eq_u32 s34, 1
	v_max_u32_e32 v76, 11, v76
	s_cselect_b64 s[24:25], -1, 0
	v_lshlrev_b32_e32 v240, 23, v76
	v_cndmask_b32_e64 v76, 2.0, 1.0, s[24:25]
	s_lshl_b32 s8, s34, 16
	v_mul_f32_e32 v230, v76, v230
	s_and_b32 s67, s8, 0x10000
	v_sub_u32_e32 v164, 0x84000000, v240
	v_pk_fma_f32 v[182:183], v[230:231], v[182:183], v[212:213] op_sel_hi:[0,1,1] neg_lo:[0,0,1] neg_hi:[0,0,1]
	v_pk_fma_f32 v[184:185], v[230:231], v[184:185], v[210:211] op_sel_hi:[0,1,1] neg_lo:[0,0,1] neg_hi:[0,0,1]
	v_pk_fma_f32 v[186:187], v[230:231], v[186:187], v[208:209] op_sel_hi:[0,1,1] neg_lo:[0,0,1] neg_hi:[0,0,1]
	v_pk_fma_f32 v[188:189], v[230:231], v[188:189], v[206:207] op_sel_hi:[0,1,1] neg_lo:[0,0,1] neg_hi:[0,0,1]
	v_fma_mixlo_f16 v78, v182, v164, 0 op_sel_hi:[0,0,0]
	v_fma_mixlo_f16 v79, v184, v164, 0 op_sel_hi:[0,0,0]
	v_fma_mixlo_f16 v80, v186, v164, 0 op_sel_hi:[0,0,0]
	v_fma_mixlo_f16 v81, v188, v164, 0 op_sel_hi:[0,0,0]
	v_lshl_add_u32 v82, v246, 4, s67
	v_fma_mixhi_f16 v78, v183, v164, 0 op_sel_hi:[0,0,0]
	v_fma_mixhi_f16 v79, v185, v164, 0 op_sel_hi:[0,0,0]
	v_fma_mixhi_f16 v80, v187, v164, 0 op_sel_hi:[0,0,0]
	v_fma_mixhi_f16 v81, v189, v164, 0 op_sel_hi:[0,0,0]
	ds_write_b128 v82, v[78:81]
	v_pk_fma_f32 v[198:199], v[230:231], v[198:199], v[196:197] op_sel_hi:[0,1,1] neg_lo:[0,0,1] neg_hi:[0,0,1]
	v_pk_fma_f32 v[200:201], v[230:231], v[200:201], v[194:195] op_sel_hi:[0,1,1] neg_lo:[0,0,1] neg_hi:[0,0,1]
	v_pk_fma_f32 v[202:203], v[230:231], v[202:203], v[192:193] op_sel_hi:[0,1,1] neg_lo:[0,0,1] neg_hi:[0,0,1]
	v_pk_fma_f32 v[204:205], v[230:231], v[204:205], v[190:191] op_sel_hi:[0,1,1] neg_lo:[0,0,1] neg_hi:[0,0,1]
	v_fma_mixlo_f16 v78, v198, v164, 0 op_sel_hi:[0,0,0]
	v_fma_mixlo_f16 v79, v200, v164, 0 op_sel_hi:[0,0,0]
	v_fma_mixlo_f16 v80, v202, v164, 0 op_sel_hi:[0,0,0]
	v_fma_mixlo_f16 v81, v204, v164, 0 op_sel_hi:[0,0,0]
	v_lshl_add_u32 v82, v247, 4, s67
	v_fma_mixhi_f16 v78, v199, v164, 0 op_sel_hi:[0,0,0]
	v_fma_mixhi_f16 v79, v201, v164, 0 op_sel_hi:[0,0,0]
	v_fma_mixhi_f16 v80, v203, v164, 0 op_sel_hi:[0,0,0]
	v_fma_mixhi_f16 v81, v205, v164, 0 op_sel_hi:[0,0,0]
	ds_write_b128 v82, v[78:81]
	v_pk_fma_f32 v[214:215], v[230:231], v[214:215], v[180:181] op_sel_hi:[0,1,1] neg_lo:[0,0,1] neg_hi:[0,0,1]
	v_pk_fma_f32 v[216:217], v[230:231], v[216:217], v[178:179] op_sel_hi:[0,1,1] neg_lo:[0,0,1] neg_hi:[0,0,1]
	v_pk_fma_f32 v[218:219], v[230:231], v[218:219], v[176:177] op_sel_hi:[0,1,1] neg_lo:[0,0,1] neg_hi:[0,0,1]
	v_pk_fma_f32 v[220:221], v[230:231], v[220:221], v[174:175] op_sel_hi:[0,1,1] neg_lo:[0,0,1] neg_hi:[0,0,1]
	v_fma_mixlo_f16 v78, v214, v164, 0 op_sel_hi:[0,0,0]
	v_fma_mixlo_f16 v79, v216, v164, 0 op_sel_hi:[0,0,0]
	v_fma_mixlo_f16 v80, v218, v164, 0 op_sel_hi:[0,0,0]
	v_fma_mixlo_f16 v81, v220, v164, 0 op_sel_hi:[0,0,0]
	v_lshl_add_u32 v82, v248, 4, s67
	v_fma_mixhi_f16 v78, v215, v164, 0 op_sel_hi:[0,0,0]
	v_fma_mixhi_f16 v79, v217, v164, 0 op_sel_hi:[0,0,0]
	v_fma_mixhi_f16 v80, v219, v164, 0 op_sel_hi:[0,0,0]
	v_fma_mixhi_f16 v81, v221, v164, 0 op_sel_hi:[0,0,0]
	ds_write_b128 v82, v[78:81]
	v_pk_fma_f32 v[222:223], v[230:231], v[222:223], v[172:173] op_sel_hi:[0,1,1] neg_lo:[0,0,1] neg_hi:[0,0,1]
	v_pk_fma_f32 v[224:225], v[230:231], v[224:225], v[170:171] op_sel_hi:[0,1,1] neg_lo:[0,0,1] neg_hi:[0,0,1]
	v_pk_fma_f32 v[226:227], v[230:231], v[226:227], v[168:169] op_sel_hi:[0,1,1] neg_lo:[0,0,1] neg_hi:[0,0,1]
	v_pk_fma_f32 v[228:229], v[230:231], v[228:229], v[166:167] op_sel_hi:[0,1,1] neg_lo:[0,0,1] neg_hi:[0,0,1]
	v_fma_mixlo_f16 v78, v222, v164, 0 op_sel_hi:[0,0,0]
	v_fma_mixlo_f16 v79, v224, v164, 0 op_sel_hi:[0,0,0]
	v_fma_mixlo_f16 v80, v226, v164, 0 op_sel_hi:[0,0,0]
	v_fma_mixlo_f16 v81, v228, v164, 0 op_sel_hi:[0,0,0]
	v_lshl_add_u32 v82, v249, 4, s67
	v_fma_mixhi_f16 v78, v223, v164, 0 op_sel_hi:[0,0,0]
	v_fma_mixhi_f16 v79, v225, v164, 0 op_sel_hi:[0,0,0]
	v_fma_mixhi_f16 v80, v227, v164, 0 op_sel_hi:[0,0,0]
	v_fma_mixhi_f16 v81, v229, v164, 0 op_sel_hi:[0,0,0]
	v_pk_mul_f32 v[206:207], v[38:39], v[74:75]
	v_pk_mul_f32 v[208:209], v[40:41], v[74:75]
	v_pk_mul_f32 v[210:211], v[34:35], v[74:75]
	v_pk_mul_f32 v[212:213], v[36:37], v[74:75]
	v_pk_mul_f32 v[190:191], v[46:47], v[74:75]
	v_pk_mul_f32 v[192:193], v[48:49], v[74:75]
	v_pk_mul_f32 v[194:195], v[42:43], v[74:75]
	v_pk_mul_f32 v[196:197], v[44:45], v[74:75]
	v_pk_mul_f32 v[174:175], v[54:55], v[74:75]
	v_pk_mul_f32 v[176:177], v[56:57], v[74:75]
	v_pk_mul_f32 v[178:179], v[50:51], v[74:75]
	v_pk_mul_f32 v[180:181], v[52:53], v[74:75]
	v_pk_mul_f32 v[166:167], v[124:125], v[74:75]
	v_pk_mul_f32 v[168:169], v[128:129], v[74:75]
	v_pk_mul_f32 v[170:171], v[126:127], v[74:75]
	v_pk_mul_f32 v[172:173], v[130:131], v[74:75]
	s_andn2_b64 vcc, exec, s[12:13]
	s_mov_b64 s[24:25], -1
	ds_write_b128 v82, v[78:81]
	s_cbranch_vccnz .LBB3_38
	s_mov_b64 s[24:25], 0

.LBB3_51:
	v_max3_f32 v74, |v182|, 0, |v183|
	v_max3_f32 v74, v74, |v184|, |v185|
	v_max3_f32 v74, v74, |v186|, |v187|
	v_max3_f32 v74, v74, |v188|, |v189|
	v_max3_f32 v74, v74, |v198|, |v199|
	v_max3_f32 v74, v74, |v200|, |v201|
	v_max3_f32 v74, v74, |v202|, |v203|
	v_max3_f32 v74, v74, |v204|, |v205|
	v_max3_f32 v74, v74, |v214|, |v215|
	v_max3_f32 v74, v74, |v216|, |v217|
	v_max3_f32 v74, v74, |v218|, |v219|
	v_max3_f32 v74, v74, |v220|, |v221|
	v_max3_f32 v74, v74, |v222|, |v223|
	v_max3_f32 v74, v74, |v224|, |v225|
	v_max3_f32 v74, v74, |v226|, |v227|
	s_waitcnt vmcnt(0)
	v_max3_f32 v74, v74, |v228|, |v229|
	v_pk_fma_f32 v[66:67], v[230:231], v[206:207], v[162:163] neg_lo:[0,0,1] neg_hi:[0,0,1]
	v_pk_fma_f32 v[68:69], v[230:231], v[208:209], v[160:161] neg_lo:[0,0,1] neg_hi:[0,0,1]
	v_max3_f32 v58, v74, |v66|, |v67|
	v_pk_fma_f32 v[70:71], v[230:231], v[210:211], v[158:159] neg_lo:[0,0,1] neg_hi:[0,0,1]
	v_max3_f32 v58, v58, |v68|, |v69|
	v_pk_fma_f32 v[72:73], v[230:231], v[212:213], v[156:157] neg_lo:[0,0,1] neg_hi:[0,0,1]
	v_max3_f32 v58, v58, |v70|, |v71|
	v_max3_f32 v63, v58, |v72|, |v73|
	v_fma_mixlo_f16 v58, v66, v164, 0 op_sel_hi:[0,0,0]
	v_fma_mixlo_f16 v59, v68, v164, 0 op_sel_hi:[0,0,0]
	v_fma_mixlo_f16 v60, v70, v164, 0 op_sel_hi:[0,0,0]
	v_fma_mixlo_f16 v61, v72, v164, 0 op_sel_hi:[0,0,0]
	v_lshl_add_u32 v62, v250, 4, s67
	v_fma_mixhi_f16 v58, v67, v164, 0 op_sel_hi:[0,0,0]
	v_fma_mixhi_f16 v59, v69, v164, 0 op_sel_hi:[0,0,0]
	v_fma_mixhi_f16 v60, v71, v164, 0 op_sel_hi:[0,0,0]
	v_fma_mixhi_f16 v61, v73, v164, 0 op_sel_hi:[0,0,0]
	ds_write_b128 v62, v[58:61]
	v_pk_fma_f32 v[74:75], v[230:231], v[190:191], v[146:147] neg_lo:[0,0,1] neg_hi:[0,0,1]
	v_pk_fma_f32 v[76:77], v[230:231], v[192:193], v[144:145] neg_lo:[0,0,1] neg_hi:[0,0,1]
	v_max3_f32 v58, v63, |v74|, |v75|
	v_pk_fma_f32 v[78:79], v[230:231], v[194:195], v[142:143] neg_lo:[0,0,1] neg_hi:[0,0,1]
	v_max3_f32 v58, v58, |v76|, |v77|
	v_pk_fma_f32 v[80:81], v[230:231], v[196:197], v[140:141] neg_lo:[0,0,1] neg_hi:[0,0,1]
	v_max3_f32 v58, v58, |v78|, |v79|
	v_max3_f32 v63, v58, |v80|, |v81|
	v_fma_mixlo_f16 v58, v74, v164, 0 op_sel_hi:[0,0,0]
	v_fma_mixhi_f16 v58, v75, v164, 0 op_sel_hi:[0,0,0]
	v_fma_mixlo_f16 v59, v76, v164, 0 op_sel_hi:[0,0,0]
	v_fma_mixlo_f16 v60, v78, v164, 0 op_sel_hi:[0,0,0]
	v_fma_mixlo_f16 v61, v80, v164, 0 op_sel_hi:[0,0,0]
	v_lshl_add_u32 v62, v251, 4, s67
	v_pk_fma_f32 v[82:83], v[230:231], v[174:175], v[138:139] neg_lo:[0,0,1] neg_hi:[0,0,1]
	v_fma_mixhi_f16 v59, v77, v164, 0 op_sel_hi:[0,0,0]
	v_fma_mixhi_f16 v60, v79, v164, 0 op_sel_hi:[0,0,0]
	v_fma_mixhi_f16 v61, v81, v164, 0 op_sel_hi:[0,0,0]
	ds_write_b128 v62, v[58:61]
	v_pk_fma_f32 v[84:85], v[230:231], v[176:177], v[136:137] neg_lo:[0,0,1] neg_hi:[0,0,1]
	v_max3_f32 v58, v63, |v82|, |v83|
	v_pk_fma_f32 v[86:87], v[230:231], v[178:179], v[134:135] neg_lo:[0,0,1] neg_hi:[0,0,1]
	v_max3_f32 v58, v58, |v84|, |v85|
	v_pk_fma_f32 v[88:89], v[230:231], v[180:181], v[132:133] neg_lo:[0,0,1] neg_hi:[0,0,1]
	v_max3_f32 v58, v58, |v86|, |v87|
	v_max3_f32 v92, v58, |v88|, |v89|
	v_pk_fma_f32 v[62:63], v[230:231], v[166:167], v[148:149] neg_lo:[0,0,1] neg_hi:[0,0,1]
	v_pk_fma_f32 v[64:65], v[230:231], v[168:169], v[150:151] neg_lo:[0,0,1] neg_hi:[0,0,1]
	v_max3_f32 v92, v92, |v62|, |v63|
	v_pk_fma_f32 v[58:59], v[230:231], v[170:171], v[152:153] neg_lo:[0,0,1] neg_hi:[0,0,1]
	v_max3_f32 v92, v92, |v64|, |v65|
	v_pk_fma_f32 v[60:61], v[230:231], v[172:173], v[154:155] neg_lo:[0,0,1] neg_hi:[0,0,1]
	v_max3_f32 v92, v92, |v58|, |v59|
	v_max3_f32 v93, v92, |v60|, |v61|
	v_mov_b32_e32 v95, v93
	v_lshl_add_u32 v94, v252, 4, s67
	v_lshl_add_u32 v96, v253, 4, s67
	v_max_f32_dpp v95, v95, v95 row_shr:1 row_mask:0xf bank_mask:0xf
	v_fma_mixlo_f16 v90, v82, v164, 0 op_sel_hi:[0,0,0]
	v_fma_mixlo_f16 v91, v84, v164, 0 op_sel_hi:[0,0,0]
	v_max_f32_dpp v95, v95, v95 row_shr:2 row_mask:0xf bank_mask:0xf
	v_fma_mixlo_f16 v92, v86, v164, 0 op_sel_hi:[0,0,0]
	v_fma_mixlo_f16 v93, v88, v164, 0 op_sel_hi:[0,0,0]
	v_max_f32_dpp v95, v95, v95 row_shr:4 row_mask:0xf bank_mask:0xf
	v_fma_mixhi_f16 v90, v83, v164, 0 op_sel_hi:[0,0,0]
	v_fma_mixhi_f16 v91, v85, v164, 0 op_sel_hi:[0,0,0]
	v_max_f32_dpp v95, v95, v95 row_shr:8 row_mask:0xf bank_mask:0xf
	v_fma_mixhi_f16 v92, v87, v164, 0 op_sel_hi:[0,0,0]
	v_fma_mixhi_f16 v93, v89, v164, 0 op_sel_hi:[0,0,0]
	v_fma_mixlo_f16 v98, v62, v164, 0 op_sel_hi:[0,0,0]
	v_fma_mixlo_f16 v99, v64, v164, 0 op_sel_hi:[0,0,0]
	v_fma_mixlo_f16 v100, v58, v164, 0 op_sel_hi:[0,0,0]
	v_fma_mixlo_f16 v101, v60, v164, 0 op_sel_hi:[0,0,0]
	v_fma_mixhi_f16 v98, v63, v164, 0 op_sel_hi:[0,0,0]
	v_fma_mixhi_f16 v99, v65, v164, 0 op_sel_hi:[0,0,0]
	v_fma_mixhi_f16 v100, v59, v164, 0 op_sel_hi:[0,0,0]
	v_fma_mixhi_f16 v101, v61, v164, 0 op_sel_hi:[0,0,0]
	ds_write_b128 v94, v[90:93]
	ds_write_b128 v96, v[98:101]
	s_lshl_b32 s19, s34, 2
	s_add_i32 s19, s19, 0x22000
	v_mov_b32_e32 v90, s19
	s_mov_b32 s24, 0x80008000
	s_mov_b32 s25, 0x80008000
	s_mov_b64 exec, s[24:25]
	ds_max_u32 v90, v95
	s_mov_b64 exec, -1
	s_mov_b64 s[24:25], -1

	.amdhsa_kernel _Z6k_rec2PKiS0_S0_PK15HIP_vector_typeIjLj4EEPKfS6_PS2_PS1_IjLj2EEPf
		.amdhsa_group_segment_fixed_size 139392
		.amdhsa_private_segment_fixed_size 0
		.amdhsa_kernarg_size 72
		.amdhsa_user_sgpr_count 2
		.amdhsa_user_sgpr_dispatch_ptr 0
		.amdhsa_user_sgpr_queue_ptr 0
		.amdhsa_user_sgpr_kernarg_segment_ptr 1
		.amdhsa_user_sgpr_dispatch_id 0
		.amdhsa_user_sgpr_kernarg_preload_length 0
		.amdhsa_user_sgpr_kernarg_preload_offset 0
		.amdhsa_user_sgpr_private_segment_size 0
		.amdhsa_uses_dynamic_stack 0
		.amdhsa_enable_private_segment 0
		.amdhsa_system_sgpr_workgroup_id_x 1
		.amdhsa_system_sgpr_workgroup_id_y 0
		.amdhsa_system_sgpr_workgroup_id_z 0
		.amdhsa_system_sgpr_workgroup_info 0
		.amdhsa_system_vgpr_workitem_id 0
		.amdhsa_next_free_vgpr 254
		.amdhsa_next_free_sgpr 96
		.amdhsa_accum_offset 256
		.amdhsa_reserve_vcc 1
		.amdhsa_float_round_mode_32 0
		.amdhsa_float_round_mode_16_64 0
		.amdhsa_float_denorm_mode_32 3
		.amdhsa_float_denorm_mode_16_64 3
		.amdhsa_dx10_clamp 1
		.amdhsa_ieee_mode 1
		.amdhsa_fp16_overflow 0
		.amdhsa_tg_split 0
		.amdhsa_exception_fp_ieee_invalid_op 0
		.amdhsa_exception_fp_denorm_src 0
		.amdhsa_exception_fp_ieee_div_zero 0
		.amdhsa_exception_fp_ieee_overflow 0
		.amdhsa_exception_fp_ieee_underflow 0
		.amdhsa_exception_fp_ieee_inexact 0
		.amdhsa_exception_int_div_zero 0
	.end_amdhsa_kernel

amdhsa.kernels:
  - .agpr_count:     0
    .args:
      - .actual_access:  read_only
        .address_space:  global
        .offset:         0
        .size:           8
        .value_kind:     global_buffer
      - .actual_access:  read_only
        .address_space:  global
        .offset:         8
        .size:           8
        .value_kind:     global_buffer
      - .actual_access:  write_only
        .address_space:  global
        .offset:         16
        .size:           8
        .value_kind:     global_buffer
      - .actual_access:  write_only
        .address_space:  global
        .offset:         24
        .size:           8
        .value_kind:     global_buffer
      - .actual_access:  write_only
        .address_space:  global
        .offset:         32
        .size:           8
        .value_kind:     global_buffer
      - .actual_access:  read_only
        .address_space:  global
        .offset:         40
        .size:           8
        .value_kind:     global_buffer
    .group_segment_fixed_size: 1024
    .kernarg_segment_align: 8
    .kernarg_segment_size: 48
    .language:       OpenCL C
    .language_version:
      - 2
      - 0
    .max_flat_workgroup_size: 1024
    .name:           _Z7k_sort2PKiPKfPiS3_S3_Pf
    .private_segment_fixed_size: 0
    .sgpr_count:     18
    .sgpr_spill_count: 0
    .symbol:         _Z7k_sort2PKiPKfPiS3_S3_Pf.kd
    .uniform_work_group_size: 1
    .uses_dynamic_stack: false
    .vgpr_count:     25
    .vgpr_spill_count: 0
    .wavefront_size: 64
  - .agpr_count:     0
    .args:
      - .actual_access:  read_only
        .address_space:  global
        .offset:         0
        .size:           8
        .value_kind:     global_buffer
      - .actual_access:  read_only
        .address_space:  global
        .offset:         8
        .size:           8
        .value_kind:     global_buffer
      - .actual_access:  read_only
        .address_space:  global
        .offset:         16
        .size:           8
        .value_kind:     global_buffer
      - .actual_access:  read_only
        .address_space:  global
        .offset:         24
        .size:           8
        .value_kind:     global_buffer
      - .actual_access:  read_only
        .address_space:  global
        .offset:         32
        .size:           8
        .value_kind:     global_buffer
      - .actual_access:  read_only
        .address_space:  global
        .offset:         40
        .size:           8
        .value_kind:     global_buffer
      - .address_space:  global
        .offset:         48
        .size:           8
        .value_kind:     global_buffer
      - .address_space:  global
        .offset:         56
        .size:           8
        .value_kind:     global_buffer
      - .offset:         64
        .size:           4
        .value_kind:     by_value
      - .offset:         68
        .size:           4
        .value_kind:     by_value
    .group_segment_fixed_size: 0
    .kernarg_segment_align: 8
    .kernarg_segment_size: 72
    .language:       OpenCL C
    .language_version:
      - 2
      - 0
    .max_flat_workgroup_size: 512
    .name:           _Z7k_spmm1PKiS0_PKfPK15HIP_vector_typeIjLj2EES0_S2_S2_Pfff
    .private_segment_fixed_size: 0
    .sgpr_count:     26
    .sgpr_spill_count: 0
    .symbol:         _Z7k_spmm1PKiS0_PKfPK15HIP_vector_typeIjLj2EES0_S2_S2_Pfff.kd
    .uniform_work_group_size: 1
    .uses_dynamic_stack: false
    .vgpr_count:     41
    .vgpr_spill_count: 0
    .wavefront_size: 64
  - .agpr_count:     0
    .args:
      - .address_space:  global
        .offset:         0
        .size:           8
        .value_kind:     global_buffer
      - .actual_access:  read_only
        .address_space:  global
        .offset:         8
        .size:           8
        .value_kind:     global_buffer
      - .actual_access:  read_only
        .address_space:  global
        .offset:         16
        .size:           8
        .value_kind:     global_buffer
      - .actual_access:  write_only
        .address_space:  global
        .offset:         24
        .size:           8
        .value_kind:     global_buffer
    .group_segment_fixed_size: 32768
    .kernarg_segment_align: 8
    .kernarg_segment_size: 32
    .language:       OpenCL C
    .language_version:
      - 2
      - 0
    .max_flat_workgroup_size: 512
    .name:           _Z7k_conv1PKfS0_S0_Pf
    .private_segment_fixed_size: 0
    .sgpr_count:     46
    .sgpr_spill_count: 0
    .symbol:         _Z7k_conv1PKfS0_S0_Pf.kd
    .uniform_work_group_size: 1
    .uses_dynamic_stack: false
    .vgpr_count:     107
    .vgpr_spill_count: 0
    .wavefront_size: 64
  - .agpr_count:     0
    .args:
      - .actual_access:  read_only
        .address_space:  global
        .offset:         0
        .size:           8
        .value_kind:     global_buffer
      - .actual_access:  read_only
        .address_space:  global
        .offset:         8
        .size:           8
        .value_kind:     global_buffer
      - .actual_access:  read_only
        .address_space:  global
        .offset:         16
        .size:           8
        .value_kind:     global_buffer
      - .address_space:  global
        .offset:         24
        .size:           8
        .value_kind:     global_buffer
      - .actual_access:  read_only
        .address_space:  global
        .offset:         32
        .size:           8
        .value_kind:     global_buffer
      - .actual_access:  read_only
        .address_space:  global
        .offset:         40
        .size:           8
        .value_kind:     global_buffer
      - .actual_access:  write_only
        .address_space:  global
        .offset:         48
        .size:           8
        .value_kind:     global_buffer
      - .actual_access:  write_only
        .address_space:  global
        .offset:         56
        .size:           8
        .value_kind:     global_buffer
      - .actual_access:  write_only
        .address_space:  global
        .offset:         64
        .size:           8
        .value_kind:     global_buffer
    .group_segment_fixed_size: 139392
    .kernarg_segment_align: 8
    .kernarg_segment_size: 72
    .language:       OpenCL C
    .language_version:
      - 2
      - 0
    .max_flat_workgroup_size: 512
    .name:           _Z6k_rec2PKiS0_S0_PK15HIP_vector_typeIjLj4EEPKfS6_PS2_PS1_IjLj2EEPf
    .private_segment_fixed_size: 0
    .sgpr_count:     75
    .sgpr_spill_count: 0
    .symbol:         _Z6k_rec2PKiS0_S0_PK15HIP_vector_typeIjLj4EEPKfS6_PS2_PS1_IjLj2EEPf.kd
    .uniform_work_group_size: 1
    .uses_dynamic_stack: false
    .vgpr_count:     254
    .vgpr_spill_count: 0
    .wavefront_size: 64
  - .agpr_count:     0
    .args:
      - .address_space:  global
        .offset:         0
        .size:           8
        .value_kind:     global_buffer
      - .address_space:  global
        .offset:         8
        .size:           8
        .value_kind:     global_buffer
      - .actual_access:  read_only
        .address_space:  global
        .offset:         16
        .size:           8
        .value_kind:     global_buffer
      - .actual_access:  read_only
        .address_space:  global
        .offset:         24
        .size:           8
        .value_kind:     global_buffer
      - .actual_access:  read_only
        .address_space:  global
        .offset:         32
        .size:           8
        .value_kind:     global_buffer
      - .actual_access:  read_only
        .address_space:  global
        .offset:         40
        .size:           8
        .value_kind:     global_buffer
      - .actual_access:  write_only
        .address_space:  global
        .offset:         48
        .size:           8
        .value_kind:     global_buffer
      - .actual_access:  write_only
        .address_space:  global
        .offset:         56
        .size:           8
        .value_kind:     global_buffer
    .group_segment_fixed_size: 127376
    .kernarg_segment_align: 8
    .kernarg_segment_size: 64
    .language:       OpenCL C
    .language_version:
      - 2
      - 0
    .max_flat_workgroup_size: 1024
    .name:           _Z7k_gemm2PK15HIP_vector_typeIjLj4EEPKS_IjLj2EEPKfS2_S2_S7_PtS8_
    .private_segment_fixed_size: 0
    .sgpr_count:     26
    .sgpr_spill_count: 0
    .symbol:         _Z7k_gemm2PK15HIP_vector_typeIjLj4EEPKS_IjLj2EEPKfS2_S2_S7_PtS8_.kd
    .uniform_work_group_size: 1
    .uses_dynamic_stack: false
    .vgpr_count:     115
    .vgpr_spill_count: 0
    .wavefront_size: 64
  - .agpr_count:     32
    .args:
      - .address_space:  global
        .offset:         0
        .size:           8
        .value_kind:     global_buffer
      - .address_space:  global
        .offset:         8
        .size:           8
        .value_kind:     global_buffer
      - .address_space:  global
        .offset:         16
        .size:           8
        .value_kind:     global_buffer
      - .actual_access:  write_only
        .address_space:  global
        .offset:         24
        .size:           8
        .value_kind:     global_buffer
    .group_segment_fixed_size: 65536
    .kernarg_segment_align: 8
    .kernarg_segment_size: 32
    .language:       OpenCL C
    .language_version:
      - 2
      - 0
    .max_flat_workgroup_size: 256
    .name:           _Z5k_fc1PKtS0_PKfPf
    .private_segment_fixed_size: 0
    .sgpr_count:     49
    .sgpr_spill_count: 0
    .symbol:         _Z5k_fc1PKtS0_PKfPf.kd
    .uniform_work_group_size: 1
    .uses_dynamic_stack: false
    .vgpr_count:     172
    .vgpr_spill_count: 0
    .wavefront_size: 64
  - .agpr_count:     0
    .args:
      - .actual_access:  read_only
        .address_space:  global
        .offset:         0
        .size:           8
        .value_kind:     global_buffer
      - .actual_access:  read_only
        .address_space:  global
        .offset:         8
        .size:           8
        .value_kind:     global_buffer
      - .actual_access:  read_only
        .address_space:  global
        .offset:         16
        .size:           8
        .value_kind:     global_buffer
      - .actual_access:  read_only
        .address_space:  global
        .offset:         24
        .size:           8
        .value_kind:     global_buffer
      - .actual_access:  write_only
        .address_space:  global
        .offset:         32
        .size:           8
        .value_kind:     global_buffer
    .group_segment_fixed_size: 2048
    .kernarg_segment_align: 8
    .kernarg_segment_size: 40
    .language:       OpenCL C
    .language_version:
      - 2
      - 0
    .max_flat_workgroup_size: 512
    .name:           _Z5k_fc2PKfS0_S0_S0_Pf
    .private_segment_fixed_size: 0
    .sgpr_count:     18
    .sgpr_spill_count: 0
    .symbol:         _Z5k_fc2PKfS0_S0_S0_Pf.kd
    .uniform_work_group_size: 1
    .uses_dynamic_stack: false
    .vgpr_count:     96
    .vgpr_spill_count: 0
    .wavefront_size: 64
  - .agpr_count:     0
    .args:
      - .actual_access:  read_only
        .address_space:  global
        .offset:         0
        .size:           8
        .value_kind:     global_buffer
      - .actual_access:  read_only
        .address_space:  global
        .offset:         8
        .size:           8
        .value_kind:     global_buffer
      - .actual_access:  read_only
        .address_space:  global
        .offset:         16
        .size:           8
        .value_kind:     global_buffer
      - .actual_access:  read_only
        .address_space:  global
        .offset:         24
        .size:           8
        .value_kind:     global_buffer
      - .actual_access:  write_only
        .address_space:  global
        .offset:         32
        .size:           8
        .value_kind:     global_buffer
      - .actual_access:  write_only
        .address_space:  global
        .offset:         40
        .size:           8
        .value_kind:     global_buffer
      - .actual_access:  write_only
        .address_space:  global
        .offset:         48
        .size:           8
        .value_kind:     global_buffer
      - .actual_access:  write_only
        .address_space:  global
        .offset:         56
        .size:           8
        .value_kind:     global_buffer
      - .actual_access:  write_only
        .address_space:  global
        .offset:         64
        .size:           8
        .value_kind:     global_buffer
    .group_segment_fixed_size: 16640
    .kernarg_segment_align: 8
    .kernarg_segment_size: 72
    .language:       OpenCL C
    .language_version:
      - 2
      - 0
    .max_flat_workgroup_size: 256
    .name:           _Z7k_prepAPKiS0_PKfS2_PiS3_PtS4_Pf
    .private_segment_fixed_size: 0
    .sgpr_count:     20
    .sgpr_spill_count: 0
    .symbol:         _Z7k_prepAPKiS0_PKfS2_PiS3_PtS4_Pf.kd
    .uniform_work_group_size: 1
    .uses_dynamic_stack: false
    .vgpr_count:     24
    .vgpr_spill_count: 0
    .wavefront_size: 64
  - .agpr_count:     0
    .args:
      - .actual_access:  read_only
        .address_space:  global
        .offset:         0
        .size:           8
        .value_kind:     global_buffer
      - .actual_access:  read_only
        .address_space:  global
        .offset:         8
        .size:           8
        .value_kind:     global_buffer
      - .actual_access:  read_only
        .address_space:  global
        .offset:         16
        .size:           8
        .value_kind:     global_buffer
      - .actual_access:  write_only
        .address_space:  global
        .offset:         24
        .size:           8
        .value_kind:     global_buffer
      - .actual_access:  write_only
        .address_space:  global
        .offset:         32
        .size:           8
        .value_kind:     global_buffer
      - .actual_access:  read_only
        .address_space:  global
        .offset:         40
        .size:           8
        .value_kind:     global_buffer
      - .actual_access:  read_only
        .address_space:  global
        .offset:         48
        .size:           8
        .value_kind:     global_buffer
      - .actual_access:  read_only
        .address_space:  global
        .offset:         56
        .size:           8
        .value_kind:     global_buffer
      - .actual_access:  read_only
        .address_space:  global
        .offset:         64
        .size:           8
        .value_kind:     global_buffer
      - .actual_access:  read_only
        .address_space:  global
        .offset:         72
        .size:           8
        .value_kind:     global_buffer
      - .actual_access:  read_only
        .address_space:  global
        .offset:         80
        .size:           8
        .value_kind:     global_buffer
      - .actual_access:  read_only
        .address_space:  global
        .offset:         88
        .size:           8
        .value_kind:     global_buffer
      - .actual_access:  write_only
        .address_space:  global
        .offset:         96
        .size:           8
        .value_kind:     global_buffer
    .group_segment_fixed_size: 0
    .kernarg_segment_align: 8
    .kernarg_segment_size: 104
    .language:       OpenCL C
    .language_version:
      - 2
      - 0
    .max_flat_workgroup_size: 256
    .name:           _Z7k_prepBPKiS0_PKfP15HIP_vector_typeIjLj2EEPiS0_S0_S2_S0_S0_S0_S2_Pj
    .private_segment_fixed_size: 0
    .sgpr_count:     21
    .sgpr_spill_count: 0
    .symbol:         _Z7k_prepBPKiS0_PKfP15HIP_vector_typeIjLj2EEPiS0_S0_S2_S0_S0_S0_S2_Pj.kd
    .uniform_work_group_size: 1
    .uses_dynamic_stack: false
    .vgpr_count:     14
    .vgpr_spill_count: 0
    .wavefront_size: 64
